# attention: pre-load landing overlapped with iteration 1 (pre->LDS write moved to iteration end, vmcnt(8) waits); prologue kn2/Q waits deferred past DMA issue
# baseline (speedup 1.0000x reference)
_Z8attn_fwdPKDF16_S0_S0_PKjPf:
	s_load_dwordx4 s[8:11], s[0:1], 0x0
	s_load_dwordx2 s[14:15], s[0:1], 0x10
	s_lshl_b32 s3, s2, 1
	s_mul_hi_u32 s4, s2, 0xaaaaaaab
	s_and_b32 s3, s3, 14
	s_lshr_b32 s4, s4, 6
	v_add_u32_e32 v1, 0xffffff00, v0
	v_readfirstlane_b32 s16, v0
	s_add_i32 s6, s3, s4
	v_cmp_gt_u32_e32 vcc, 48, v1
	s_and_saveexec_b64 s[12:13], vcc
	s_cbranch_execz .LBB2_2
	s_load_dwordx2 s[4:5], s[0:1], 0x18
	v_mad_u64_u32 v[2:3], s[18:19], s6, 48, v[0:1]
	v_mov_b32_e32 v3, 0
	s_mov_b32 s3, 0xf800000
	s_waitcnt lgkmcnt(0)
	v_lshl_add_u64 v[2:3], v[2:3], 2, s[4:5]
	global_load_dword v209, v[2:3], off offset:-1024
.LBB2_2:
	s_or_b64 exec, exec, s[12:13]
	s_lshr_b32 s2, s2, 3
	s_mul_hi_u32 s3, s2, 0x15555556
	s_mul_i32 s3, s3, 12
	s_lshr_b32 s19, s16, 6
	s_sub_i32 s20, s2, s3
	s_lshl_b32 s18, s19, 5
	s_mul_i32 s3, s6, 0xc00
	s_lshl_b32 s4, s20, 8
	v_and_b32_e32 v162, 31, v0
	s_mul_hi_u32 s2, s6, 0xc00
	s_add_u32 s12, s3, s4
	v_or_b32_e32 v2, s18, v162
	s_addc_u32 s13, s2, 0
	v_mov_b32_e32 v3, 0
	v_lshl_add_u64 v[4:5], s[12:13], 0, v[2:3]
	v_bfe_u32 v1, v0, 5, 1
	v_lshlrev_b64 v[4:5], 7, v[4:5]
	s_waitcnt lgkmcnt(0)
	v_lshl_add_u64 v[4:5], s[8:9], 0, v[4:5]
	v_lshlrev_b32_e32 v148, 4, v1
	v_mov_b32_e32 v149, v3
	v_lshl_add_u64 v[4:5], v[4:5], 0, v[148:149]
	global_load_dwordx4 v[96:99], v[4:5], off nt
	global_load_dwordx4 v[100:103], v[4:5], off offset:32 nt
	global_load_dwordx4 v[104:107], v[4:5], off offset:64 nt
	global_load_dwordx4 v[108:111], v[4:5], off offset:96 nt
	s_sub_u32 s44, s10, s8
	s_subb_u32 s45, s11, s9
	s_add_i32 s46, s20, 2
	s_cmp_gt_u32 s46, 11
	s_cselect_b32 s47, 12, 0
	s_sub_i32 s46, s46, s47
	s_mov_b32 s42, s46
	s_sub_i32 s46, s46, s20
	s_lshl_b32 s46, s46, 15
	s_ashr_i32 s47, s46, 31
	s_add_u32 s46, s46, s44
	s_addc_u32 s47, s47, s45
	v_lshl_add_u64 v[202:203], v[4:5], 0, s[46:47]
	s_add_i32 s46, s20, 10
	s_cmp_gt_u32 s46, 11
	s_cselect_b32 s47, 12, 0
	s_sub_i32 s46, s46, s47
	s_mov_b32 s43, s46
	s_sub_i32 s46, s46, s20
	s_lshl_b32 s46, s46, 15
	s_ashr_i32 s47, s46, 31
	s_add_u32 s46, s46, s44
	s_addc_u32 s47, s47, s45
	v_lshl_add_u64 v[204:205], v[4:5], 0, s[46:47]
	v_bfe_u32 v6, v0, 3, 3
	s_mul_i32 s2, s6, 0x60000
	v_lshl_or_b32 v6, s19, 3, v6
	s_mov_b32 s7, 0
	s_mul_hi_u32 s3, s6, 0x60000
	v_mov_b32_e32 v9, v3
	v_mov_b32_e32 v11, v3
	v_mov_b32_e32 v7, v3
	v_lshrrev_b32_e32 v3, 1, v6
	s_add_u32 s2, s10, s2
	v_xor_b32_e32 v3, v3, v0
	s_addc_u32 s3, s11, s3
	s_lshl_b64 s[4:5], s[6:7], 6
	s_movk_i32 s8, 0x1800
	v_mov_b64_e32 v[4:5], s[14:15]
	v_lshlrev_b32_e32 v8, 7, v6
	v_lshlrev_b32_e32 v3, 4, v3
	v_lshl_add_u64 v[6:7], s[4:5], 0, v[6:7]
	v_and_b32_e32 v10, 0x70, v3
	v_lshl_add_u64 v[8:9], s[2:3], 0, v[8:9]
	v_mad_u64_u32 v[4:5], s[2:3], v6, s8, v[4:5]
	s_lshl_b32 s9, s20, 2
	s_lshl_b32 s6, s20, 15
	v_lshl_add_u64 v[150:151], v[8:9], 0, v[10:11]
	v_mad_u32_u24 v5, v7, s8, v5
	s_or_b32 s4, s9, 1
	v_lshl_add_u64 v[6:7], v[150:151], 0, s[6:7]
	s_lshl_b32 s6, s20, 9
	v_lshl_add_u64 v[152:153], v[4:5], 0, v[10:11]
	v_lshl_add_u64 v[4:5], v[152:153], 0, s[6:7]
	s_lshl_b32 s6, s4, 13
	s_or_b32 s5, s9, 2
	v_lshl_add_u64 v[8:9], v[150:151], 0, s[6:7]
	s_lshl_b32 s6, s4, 7
	v_lshl_add_u64 v[10:11], v[152:153], 0, s[6:7]
	s_lshl_b32 s6, s5, 13
	s_or_b32 s17, s9, 3
	v_lshl_add_u64 v[12:13], v[150:151], 0, s[6:7]
	s_lshl_b32 s6, s5, 7
	s_lshl_b32 s21, s19, 10
	v_lshl_add_u64 v[14:15], v[152:153], 0, s[6:7]
	s_lshl_b32 s6, s17, 13
	s_add_i32 s22, s21, 0x2000
	s_add_i32 s10, s21, 0x4000
	s_add_i32 s11, s21, 0x6000
	s_add_i32 s14, s21, 0x8000
	s_add_i32 s15, s21, 0xa000
	s_add_i32 s23, s21, 0xc000
	s_add_i32 s24, s21, 0xe000
	v_lshl_add_u64 v[16:17], v[150:151], 0, s[6:7]
	s_lshl_b32 s6, s17, 7
	s_cmp_gt_u32 s20, 10
	s_cselect_b32 s2, -11, 1
	s_add_i32 s2, s2, s20
	v_lshl_add_u64 v[18:19], v[152:153], 0, s[6:7]
	s_lshl_b32 s6, s2, 2
	s_lshl_b64 s[4:5], s[6:7], 13
	v_lshl_add_u64 v[20:21], v[150:151], 0, s[4:5]
	s_add_i32 s3, s21, 0x10000
	s_lshl_b32 s2, s2, 9
	s_add_i32 s9, s9, -4
	v_and_b32_e32 v149, 15, v0
	s_mov_b32 s4, m0
	s_mov_b32 m0, s21
	s_nop 0
	global_load_lds_dwordx4 v[6:7], off
	s_mov_b32 m0, s4
	s_nop 0
	s_mov_b32 s4, m0
	s_mov_b32 m0, s22
	s_nop 0
	global_load_lds_dwordx4 v[4:5], off
	s_mov_b32 m0, s4
	s_nop 0
	s_mov_b32 s4, m0
	s_mov_b32 m0, s10
	s_nop 0
	global_load_lds_dwordx4 v[8:9], off
	s_mov_b32 m0, s4
	s_nop 0
	s_mov_b32 s4, m0
	s_mov_b32 m0, s11
	s_nop 0
	global_load_lds_dwordx4 v[10:11], off
	s_mov_b32 m0, s4
	s_nop 0
	s_mov_b32 s4, m0
	s_mov_b32 m0, s14
	s_nop 0
	global_load_lds_dwordx4 v[12:13], off
	s_mov_b32 m0, s4
	s_nop 0
	s_mov_b32 s4, m0
	s_mov_b32 m0, s15
	s_nop 0
	global_load_lds_dwordx4 v[14:15], off
	s_mov_b32 m0, s4
	s_nop 0
	s_mov_b32 s4, m0
	s_mov_b32 m0, s23
	s_nop 0
	global_load_lds_dwordx4 v[16:17], off
	s_mov_b32 m0, s4
	s_nop 0
	s_mov_b32 s4, m0
	s_mov_b32 m0, s24
	s_nop 0
	global_load_lds_dwordx4 v[18:19], off
	s_mov_b32 m0, s4
	s_nop 0
	s_mov_b32 s4, m0
	s_mov_b32 m0, s3
	s_nop 0
	global_load_lds_dwordx4 v[20:21], off
	s_mov_b32 m0, s4
	s_mov_b32 s3, s7
	v_lshl_add_u64 v[4:5], v[152:153], 0, s[2:3]
	s_add_i32 s2, s21, 0x12000
	s_mov_b32 s3, m0
	s_mov_b32 m0, s2
	s_nop 0
	global_load_lds_dwordx4 v[4:5], off
	s_mov_b32 m0, s3
	s_or_b32 s2, s6, 1
	s_mov_b32 s3, s7
	s_lshl_b64 s[4:5], s[2:3], 13
	s_add_i32 s3, s21, 0x14000
	v_lshl_add_u64 v[4:5], v[150:151], 0, s[4:5]
	s_mov_b32 s4, m0
	s_mov_b32 m0, s3
	s_nop 0
	global_load_lds_dwordx4 v[4:5], off
	s_mov_b32 m0, s4
	s_lshl_b32 s2, s2, 7
	s_mov_b32 s3, s7
	v_lshl_add_u64 v[4:5], v[152:153], 0, s[2:3]
	s_add_i32 s2, s21, 0x16000
	s_mov_b32 s3, m0
	s_mov_b32 m0, s2
	s_nop 0
	global_load_lds_dwordx4 v[4:5], off
	s_mov_b32 m0, s3
	s_or_b32 s2, s6, 2
	s_mov_b32 s3, s7
	s_lshl_b64 s[4:5], s[2:3], 13
	s_add_i32 s3, s21, 0x18000
	v_lshl_add_u64 v[4:5], v[150:151], 0, s[4:5]
	s_mov_b32 s4, m0
	s_mov_b32 m0, s3
	s_nop 0
	global_load_lds_dwordx4 v[4:5], off
	s_mov_b32 m0, s4
	s_lshl_b32 s2, s2, 7
	s_mov_b32 s3, s7
	v_lshl_add_u64 v[4:5], v[152:153], 0, s[2:3]
	s_add_i32 s2, s21, 0x1a000
	s_mov_b32 s3, m0
	s_mov_b32 m0, s2
	s_nop 0
	global_load_lds_dwordx4 v[4:5], off
	s_mov_b32 m0, s3
	s_or_b32 s6, s6, 3
	s_lshl_b64 s[2:3], s[6:7], 13
	v_lshl_add_u64 v[4:5], v[150:151], 0, s[2:3]
	s_add_i32 s2, s21, 0x1c000
	s_mov_b32 s3, m0
	s_mov_b32 m0, s2
	s_nop 0
	global_load_lds_dwordx4 v[4:5], off
	s_mov_b32 m0, s3
	s_lshl_b32 s6, s6, 7
	s_add_i32 s2, s21, 0x1e000
	s_cmp_lg_u32 s20, 0
	v_lshl_add_u64 v[4:5], v[152:153], 0, s[6:7]
	s_mov_b32 s3, m0
	s_mov_b32 m0, s2
	s_nop 0
	global_load_lds_dwordx4 v[4:5], off
	s_mov_b32 m0, s3
	s_cselect_b32 s2, s9, 44
	s_ashr_i32 s3, s2, 31
	s_lshl_b64 s[4:5], s[2:3], 13
	v_lshl_add_u64 v[4:5], v[150:151], 0, s[4:5]
	s_lshl_b32 s4, s2, 6
	s_ashr_i32 s5, s4, 31
	global_load_dwordx4 v[210:213], v[202:203], off
	global_load_dwordx4 v[214:217], v[202:203], off offset:32
	global_load_dwordx4 v[218:221], v[202:203], off offset:64
	global_load_dwordx4 v[222:225], v[202:203], off offset:96
	global_load_dwordx4 v[226:229], v[204:205], off
	global_load_dwordx4 v[230:233], v[204:205], off offset:32
	global_load_dwordx4 v[234:237], v[204:205], off offset:64
	global_load_dwordx4 v[238:241], v[204:205], off offset:96
	global_load_dwordx4 v[112:115], v[4:5], off
	v_lshl_add_u64 v[4:5], s[4:5], 1, v[152:153]
	s_or_b32 s4, s2, 1
	s_ashr_i32 s5, s4, 31
	s_lshl_b64 s[6:7], s[4:5], 13
	s_lshl_b32 s4, s4, 6
	global_load_dwordx4 v[116:119], v[4:5], off
	v_lshl_add_u64 v[4:5], v[150:151], 0, s[6:7]
	s_ashr_i32 s5, s4, 31
	global_load_dwordx4 v[120:123], v[4:5], off
	v_lshl_add_u64 v[4:5], s[4:5], 1, v[152:153]
	s_or_b32 s4, s2, 2
	s_ashr_i32 s5, s4, 31
	s_lshl_b64 s[6:7], s[4:5], 13
	s_lshl_b32 s4, s4, 6
	s_or_b32 s2, s2, 3
	global_load_dwordx4 v[124:127], v[4:5], off
	v_lshl_add_u64 v[4:5], v[150:151], 0, s[6:7]
	s_ashr_i32 s5, s4, 31
	s_ashr_i32 s3, s2, 31
	global_load_dwordx4 v[128:131], v[4:5], off
	v_lshl_add_u64 v[4:5], s[4:5], 1, v[152:153]
	s_lshl_b64 s[4:5], s[2:3], 13
	s_lshl_b32 s2, s2, 6
	global_load_dwordx4 v[132:135], v[4:5], off
	v_lshl_add_u64 v[4:5], v[150:151], 0, s[4:5]
	s_ashr_i32 s3, s2, 31
	global_load_dwordx4 v[136:139], v[4:5], off
	v_lshl_add_u64 v[4:5], s[2:3], 1, v[152:153]
	global_load_dwordx4 v[140:143], v[4:5], off
	s_movk_i32 s2, 0xbf
	v_cmp_lt_u32_e32 vcc, s2, v0
	s_and_saveexec_b64 s[2:3], vcc
	s_xor_b64 s[2:3], exec, s[2:3]
	v_and_b32_e32 v149, 15, v0
	s_or_saveexec_b64 s[4:5], s[2:3]
	v_and_b32_e32 v163, 63, v0
	s_xor_b64 exec, exec, s[4:5]
	s_cbranch_execz .LBB2_6
	v_lshrrev_b32_e32 v3, 4, v0
	v_cvt_f32_ubyte0_e32 v3, v3
	v_mul_f32_e32 v3, 0x3d4ccccd, v3
	v_mov_b32_e32 v4, 0x3d4ccccd
	v_cmp_lt_u32_e32 vcc, 15, v0
	s_mov_b32 s2, 0xf800000
	s_nop 0
	v_cndmask_b32_e32 v3, v4, v3, vcc
	v_mul_f32_e32 v4, 0x3e80adfd, v3
	v_mul_f32_e32 v5, 0x4f800000, v4
	v_cmp_gt_f32_e32 vcc, s2, v4
	v_mul_f32_e32 v3, 0xbda3d70a, v3
	s_nop 0
	v_cndmask_b32_e32 v4, v4, v5, vcc
	v_sqrt_f32_e32 v5, v4
	s_nop 0
	v_add_u32_e32 v6, -1, v5
	v_fma_f32 v7, -v6, v5, v4
	v_cmp_ge_f32_e64 s[2:3], 0, v7
	v_add_u32_e32 v7, 1, v5
	s_nop 0
	v_cndmask_b32_e64 v6, v5, v6, s[2:3]
	v_fma_f32 v5, -v7, v5, v4
	v_cmp_lt_f32_e64 s[2:3], 0, v5
	s_nop 1
	v_cndmask_b32_e64 v5, v6, v7, s[2:3]
	v_mul_f32_e32 v6, 0x37800000, v5
	v_cndmask_b32_e32 v5, v5, v6, vcc
	v_mov_b32_e32 v6, 0x260
	v_cmp_class_f32_e32 vcc, v4, v6
	s_nop 1
	v_cndmask_b32_e32 v4, v5, v4, vcc
	v_div_scale_f32 v5, s[2:3], v4, v4, 1.0
	v_rcp_f32_e32 v6, v5
	s_nop 0
	v_fma_f32 v7, -v5, v6, 1.0
	v_fmac_f32_e32 v6, v7, v6
	v_div_scale_f32 v7, vcc, 1.0, v4, 1.0
	v_mul_f32_e32 v8, v7, v6
	v_fma_f32 v9, -v5, v8, v7
	v_fmac_f32_e32 v8, v9, v6
	v_mul_u32_u24_e32 v9, v149, v149
	v_cvt_f32_ubyte0_e32 v9, v9
	v_div_scale_f32 v10, s[2:3], v3, v3, v9
	v_rcp_f32_e32 v11, v10
	v_fma_f32 v5, -v5, v8, v7
	v_div_fmas_f32 v5, v5, v6, v8
	s_mov_b32 s2, 0x3fb8aa3b
	v_fma_f32 v6, -v10, v11, 1.0
	v_fmac_f32_e32 v11, v6, v11
	v_div_scale_f32 v6, vcc, v9, v3, v9
	v_mul_f32_e32 v7, v6, v11
	v_fma_f32 v8, -v10, v7, v6
	v_fmac_f32_e32 v7, v8, v11
	v_fma_f32 v6, -v10, v7, v6
	v_div_fmas_f32 v6, v6, v11, v7
	v_div_fixup_f32 v3, v6, v3, v9
	v_mul_f32_e32 v6, 0x3fb8aa3b, v3
	v_fma_f32 v7, v3, s2, -v6
	v_rndne_f32_e32 v8, v6
	v_fmamk_f32 v7, v3, 0x32a5705f, v7
	v_sub_f32_e32 v6, v6, v8
	v_add_f32_e32 v6, v6, v7
	v_exp_f32_e32 v6, v6
	v_cvt_i32_f32_e32 v7, v8
	s_mov_b32 s2, 0xc2ce8ed0
	v_div_fixup_f32 v4, v5, v4, 1.0
	v_cmp_ngt_f32_e32 vcc, s2, v3
	v_ldexp_f32 v5, v6, v7
	s_mov_b32 s2, 0x42b17218
	v_cndmask_b32_e32 v5, 0, v5, vcc
	v_mov_b32_e32 v6, 0x7f800000
	v_cmp_nlt_f32_e32 vcc, s2, v3
	s_nop 1
	v_cndmask_b32_e32 v3, v6, v5, vcc
	v_mul_f32_e32 v5, v4, v3
	v_mul_f32_e32 v4, v4, v5
	v_lshlrev_b32_e32 v5, 2, v0
	v_mul_f32_e32 v4, 0x3fb8aa3b, v4
	v_or_b32_e32 v6, 0x20000, v5
	ds_write_b32 v6, v4
	v_add_u32_e32 v4, 0x20300, v5
	ds_write_b32 v4, v3
.LBB2_6:
	s_or_b64 exec, exec, s[4:5]
	s_waitcnt vmcnt(32)
	v_add_u32_e32 v194, 0xffffff00, v0
	v_cmp_gt_u32_e32 vcc, 48, v194
	s_and_saveexec_b64 s[36:37], vcc
	s_cbranch_execz .Lattn_knl_done
	s_mov_b32 s40, 0xf800000
	v_mov_b32_e32 v195, 0x260
	v_mov_b32_e32 v196, 0x20200
	v_mul_f32_e32 v194, 0x4f800000, v209
	v_cmp_gt_f32_e32 vcc, s40, v209
	s_nop 1
	v_cndmask_b32_e32 v209, v209, v194, vcc
	v_sqrt_f32_e32 v194, v209
	s_nop 0
	v_add_u32_e32 v197, -1, v194
	v_add_u32_e32 v198, 1, v194
	v_fma_f32 v199, -v197, v194, v209
	v_fma_f32 v200, -v198, v194, v209
	v_cmp_ge_f32_e64 s[38:39], 0, v199
	s_nop 1
	v_cndmask_b32_e64 v194, v194, v197, s[38:39]
	v_cmp_lt_f32_e64 s[38:39], 0, v200
	s_nop 1
	v_cndmask_b32_e64 v194, v194, v198, s[38:39]
	v_mul_f32_e32 v197, 0x37800000, v194
	v_cndmask_b32_e32 v194, v194, v197, vcc
	v_cmp_class_f32_e32 vcc, v209, v195
	s_nop 1
	v_cndmask_b32_e32 v209, v194, v209, vcc
	v_mul_f32_e32 v209, 0x3f800347, v209
	v_lshl_add_u32 v194, v0, 2, v196
	ds_write_b32 v194, v209
.Lattn_knl_done:
	s_or_b64 exec, exec, s[36:37]
	v_fma_mix_f32 v3, v96, v96, 0 op_sel_hi:[1,1,0]
	v_mbcnt_lo_u32_b32 v4, -1, 0
	v_fma_mix_f32 v3, v96, v96, v3 op_sel:[1,1,0] op_sel_hi:[1,1,0]
	v_mbcnt_hi_u32_b32 v4, -1, v4
	v_fma_mix_f32 v3, v97, v97, v3 op_sel_hi:[1,1,0]
	v_and_b32_e32 v6, 64, v4
	v_fma_mix_f32 v3, v97, v97, v3 op_sel:[1,1,0] op_sel_hi:[1,1,0]
	v_xor_b32_e32 v5, 32, v4
	v_fma_mix_f32 v3, v98, v98, v3 op_sel_hi:[1,1,0]
	v_add_u32_e32 v6, 64, v6
	v_fma_mix_f32 v3, v98, v98, v3 op_sel:[1,1,0] op_sel_hi:[1,1,0]
	v_cmp_lt_i32_e32 vcc, v5, v6
	v_fma_mix_f32 v3, v99, v99, v3 op_sel_hi:[1,1,0]
	s_mov_b32 s2, 0xf800000
	v_fma_mix_f32 v3, v99, v99, v3 op_sel:[1,1,0] op_sel_hi:[1,1,0]
	v_cndmask_b32_e32 v5, v4, v5, vcc
	v_fma_mix_f32 v3, v100, v100, v3 op_sel_hi:[1,1,0]
	v_lshlrev_b32_e32 v5, 2, v5
	v_fma_mix_f32 v3, v100, v100, v3 op_sel:[1,1,0] op_sel_hi:[1,1,0]
	s_load_dwordx2 s[8:9], s[0:1], 0x20
	v_fma_mix_f32 v3, v101, v101, v3 op_sel_hi:[1,1,0]
	s_mov_b32 s23, 0
	v_fma_mix_f32 v3, v101, v101, v3 op_sel:[1,1,0] op_sel_hi:[1,1,0]
	s_nop 0
	v_fma_mix_f32 v3, v102, v102, v3 op_sel_hi:[1,1,0]
	s_nop 0
	v_fma_mix_f32 v3, v102, v102, v3 op_sel:[1,1,0] op_sel_hi:[1,1,0]
	s_nop 0
	v_fma_mix_f32 v3, v103, v103, v3 op_sel_hi:[1,1,0]
	s_nop 0
	v_fma_mix_f32 v3, v103, v103, v3 op_sel:[1,1,0] op_sel_hi:[1,1,0]
	s_nop 0
	v_fma_mix_f32 v3, v104, v104, v3 op_sel_hi:[1,1,0]
	s_nop 0
	v_fma_mix_f32 v3, v104, v104, v3 op_sel:[1,1,0] op_sel_hi:[1,1,0]
	s_nop 0
	v_fma_mix_f32 v3, v105, v105, v3 op_sel_hi:[1,1,0]
	s_nop 0
	v_fma_mix_f32 v3, v105, v105, v3 op_sel:[1,1,0] op_sel_hi:[1,1,0]
	s_nop 0
	v_fma_mix_f32 v3, v106, v106, v3 op_sel_hi:[1,1,0]
	s_nop 0
	v_fma_mix_f32 v3, v106, v106, v3 op_sel:[1,1,0] op_sel_hi:[1,1,0]
	s_nop 0
	v_fma_mix_f32 v3, v107, v107, v3 op_sel_hi:[1,1,0]
	s_nop 0
	v_fma_mix_f32 v3, v107, v107, v3 op_sel:[1,1,0] op_sel_hi:[1,1,0]
	s_nop 0
	v_fma_mix_f32 v3, v108, v108, v3 op_sel_hi:[1,1,0]
	s_nop 0
	v_fma_mix_f32 v3, v108, v108, v3 op_sel:[1,1,0] op_sel_hi:[1,1,0]
	s_nop 0
	v_fma_mix_f32 v3, v109, v109, v3 op_sel_hi:[1,1,0]
	s_nop 0
	v_fma_mix_f32 v3, v109, v109, v3 op_sel:[1,1,0] op_sel_hi:[1,1,0]
	s_nop 0
	v_fma_mix_f32 v3, v110, v110, v3 op_sel_hi:[1,1,0]
	s_nop 0
	v_fma_mix_f32 v3, v110, v110, v3 op_sel:[1,1,0] op_sel_hi:[1,1,0]
	s_nop 0
	v_fma_mix_f32 v3, v111, v111, v3 op_sel_hi:[1,1,0]
	s_nop 0
	v_fma_mix_f32 v3, v111, v111, v3 op_sel:[1,1,0] op_sel_hi:[1,1,0]
	ds_bpermute_b32 v5, v5, v3
	s_waitcnt lgkmcnt(0)
	v_add_f32_e32 v3, v3, v5
	v_xor_b32_e32 v5, 1, v4
	v_cmp_lt_i32_e32 vcc, v5, v6
	s_nop 1
	v_cndmask_b32_e32 v5, v4, v5, vcc
	v_lshlrev_b32_e32 v164, 2, v5
	ds_bpermute_b32 v5, v164, v3
	s_waitcnt lgkmcnt(0)
	v_max_f32_e32 v5, v5, v5
	v_max_f32_e32 v3, v3, v5
	v_xor_b32_e32 v5, 2, v4
	v_cmp_lt_i32_e32 vcc, v5, v6
	s_nop 1
	v_cndmask_b32_e32 v5, v4, v5, vcc
	v_lshlrev_b32_e32 v165, 2, v5
	ds_bpermute_b32 v5, v165, v3
	s_waitcnt lgkmcnt(0)
	v_max_f32_e32 v5, v5, v5
	v_max_f32_e32 v3, v3, v5
	v_xor_b32_e32 v5, 4, v4
	v_cmp_lt_i32_e32 vcc, v5, v6
	s_nop 1
	v_cndmask_b32_e32 v5, v4, v5, vcc
	v_lshlrev_b32_e32 v166, 2, v5
	ds_bpermute_b32 v5, v166, v3
	s_waitcnt lgkmcnt(0)
	v_max_f32_e32 v5, v5, v5
	v_max_f32_e32 v3, v3, v5
	v_xor_b32_e32 v5, 8, v4
	v_cmp_lt_i32_e32 vcc, v5, v6
	s_nop 1
	v_cndmask_b32_e32 v5, v4, v5, vcc
	v_lshlrev_b32_e32 v167, 2, v5
	ds_bpermute_b32 v5, v167, v3
	s_waitcnt lgkmcnt(0)
	v_max_f32_e32 v5, v5, v5
	v_max_f32_e32 v3, v3, v5
	v_xor_b32_e32 v5, 16, v4
	v_cmp_lt_i32_e32 vcc, v5, v6
	s_nop 1
	v_cndmask_b32_e32 v4, v4, v5, vcc
	v_lshlrev_b32_e32 v168, 2, v4
	ds_bpermute_b32 v4, v168, v3
	s_waitcnt lgkmcnt(0)
	v_max_f32_e32 v4, v4, v4
	v_max_f32_e32 v3, v3, v4
	v_mul_f32_e32 v4, 0x4f800000, v3
	v_cmp_gt_f32_e32 vcc, s2, v3
	s_nop 1
	v_cndmask_b32_e32 v3, v3, v4, vcc
	v_sqrt_f32_e32 v4, v3
	s_nop 0
	v_add_u32_e32 v5, -1, v4
	v_fma_f32 v6, -v5, v4, v3
	v_cmp_ge_f32_e64 s[0:1], 0, v6
	v_add_u32_e32 v6, 1, v4
	s_nop 0
	v_cndmask_b32_e64 v5, v4, v5, s[0:1]
	v_fma_f32 v4, -v6, v4, v3
	v_cmp_lt_f32_e64 s[0:1], 0, v4
	s_nop 1
	v_cndmask_b32_e64 v4, v5, v6, s[0:1]
	v_mul_f32_e32 v5, 0x37800000, v4
	v_cndmask_b32_e32 v4, v4, v5, vcc
	v_mov_b32_e32 v5, 0x260
	v_cmp_class_f32_e32 vcc, v3, v5
	s_nop 1
	v_cndmask_b32_e32 v3, v4, v3, vcc
	v_cmp_eq_u32_e32 vcc, 0, v163
	v_readfirstlane_b32 s0, v3
	v_mov_b32_e32 v3, 0x3f800347
	s_nop 0
	v_mul_f32_e32 v169, s0, v3
	s_and_saveexec_b64 s[0:1], vcc
	s_lshl_b32 s2, s19, 2
	s_add_i32 s2, s2, 0x206c0
	v_mov_b32_e32 v3, s2
	ds_write_b32 v3, v169
	s_or_b64 exec, exec, s[0:1]
	v_lshrrev_b32_e32 v4, 1, v0
	v_lshlrev_b32_e32 v3, 7, v162
	v_bfe_u32 v5, v0, 1, 3
	v_bitop3_b32 v4, v1, v4, 7 bitop3:0x78
	v_lshl_or_b32 v170, v4, 4, v3
	v_bitop3_b32 v4, v1, v5, 2 bitop3:0x36
	v_lshl_or_b32 v171, v4, 4, v3
	v_bitop3_b32 v4, v1, v5, 4 bitop3:0x36
	v_lshl_or_b32 v172, v4, 4, v3
	v_bitop3_b32 v4, v1, v5, 6 bitop3:0x36
	v_lshrrev_b32_e32 v174, 4, v2
	v_add_u32_e32 v2, s20, v163
	v_lshl_or_b32 v173, v4, 4, v3
	v_add_u32_e32 v3, -12, v2
	v_min_u32_e32 v2, v3, v2
	v_cmp_gt_u32_e32 vcc, 12, v2
	v_cmp_gt_u32_e64 s[2:3], 48, v163
	v_lshlrev_b32_e32 v175, 4, v0
	v_cndmask_b32_e32 v2, 0, v2, vcc
	v_sub_u32_e32 v3, s20, v2
	v_sub_u32_e32 v4, 0, v3
	v_max_i32_e32 v3, v3, v4
	v_add_u32_e32 v4, -2, v163
	v_lshlrev_b32_e32 v0, 2, v1
	v_cndmask_b32_e64 v1, 0, v163, s[2:3]
	v_cmp_gt_u32_e64 s[0:1], 10, v4
	v_lshrrev_b32_e32 v4, 2, v1
	v_min_u32_e32 v5, s20, v4
	v_max_u32_e32 v4, s20, v4
	v_lshlrev_b32_e32 v1, 2, v1
	v_sub_u32_e32 v4, v4, v5
	v_and_b32_e32 v5, 12, v1
	s_lshl_b32 s4, s19, 1
	v_xad_u32 v6, s4, -1, v5
	v_sub_u32_e32 v5, s4, v5
	v_add_u32_e32 v5, -3, v5
	v_max3_i32 v5, v6, v5, 0
	v_or_b32_e32 v176, 0x20600, v1
	v_lshlrev_b32_e32 v1, 6, v4
	v_lshlrev_b32_e32 v4, 2, v5
	s_mov_b32 s4, 0x20000
	v_add3_u32 v177, v1, v4, s4
	v_min_u32_e32 v1, v0, v149
	v_max_u32_e32 v4, v0, v149
	v_sub_u32_e32 v178, v4, v1
	v_or_b32_e32 v1, 1, v0
	v_min_u32_e32 v4, v1, v149
	v_max_u32_e32 v1, v1, v149
	v_sub_u32_e32 v179, v1, v4
	v_or_b32_e32 v1, 2, v0
	v_min_u32_e32 v4, v1, v149
	v_max_u32_e32 v1, v1, v149
	v_sub_u32_e32 v180, v1, v4
	v_or_b32_e32 v1, 3, v0
	v_min_u32_e32 v4, v1, v149
	v_max_u32_e32 v1, v1, v149
	v_sub_u32_e32 v181, v1, v4
	v_or_b32_e32 v1, 8, v0
	v_min_u32_e32 v4, v1, v149
	v_max_u32_e32 v1, v1, v149
	v_sub_u32_e32 v182, v1, v4
	v_or_b32_e32 v1, 9, v0
	v_min_u32_e32 v4, v1, v149
	v_max_u32_e32 v1, v1, v149
	v_sub_u32_e32 v183, v1, v4
	v_or_b32_e32 v1, 10, v0
	v_min_u32_e32 v4, v1, v149
	v_max_u32_e32 v1, v1, v149
	v_or_b32_e32 v0, 11, v0
	v_mov_b32_e32 v32, 0
	v_lshlrev_b32_e32 v2, 4, v2
	v_lshlrev_b32_e32 v3, 6, v3
	v_sub_u32_e32 v184, v1, v4
	v_min_u32_e32 v1, v0, v149
	v_max_u32_e32 v0, v0, v149
	v_mov_b32_e32 v33, v32
	v_mov_b32_e32 v46, v32
	v_mov_b32_e32 v47, v32
	s_lshl_b32 s25, s19, 2
	v_sub_u32_e32 v185, v0, v1
	v_mov_b32_e32 v34, v32
	v_mov_b32_e32 v35, v32
	v_mov_b32_e32 v36, v32
	v_mov_b32_e32 v37, v32
	v_mov_b32_e32 v38, v32
	v_mov_b32_e32 v39, v32
	v_mov_b32_e32 v40, v32
	v_mov_b32_e32 v41, v32
	v_mov_b32_e32 v42, v32
	v_mov_b32_e32 v43, v32
	v_mov_b32_e32 v44, v32
	v_mov_b32_e32 v45, v32
	v_add_u32_e32 v190, 0x20600, v2
	v_add_u32_e32 v191, 0x20000, v3
	v_mov_b64_e32 v[62:63], v[46:47]
	v_mov_b64_e32 v[0:1], v[32:33]
	v_mov_b64_e32 v[16:17], v[32:33]
	s_lshr_b32 s24, s16, 7
	s_add_i32 s25, s25, 0x206e0
	v_mov_b32_e32 v154, v32
	v_mov_b32_e32 v155, v32
	v_mov_b32_e32 v156, v32
	v_mov_b32_e32 v157, v32
	v_mov_b32_e32 v158, v32
	v_mov_b32_e32 v159, v32
	v_mov_b32_e32 v160, v32
	v_mov_b32_e32 v161, v32
	s_mov_b64 s[10:11], -1
	s_mov_b64 s[6:7], 0
	s_mov_b32 s33, 0xff61b1e6
	v_mov_b32_e32 v193, 0xff61b1e6
	v_mov_b32_e32 v186, 0x206c0
	v_mov_b32_e32 v187, 0x206e0
	v_mov_b32_e32 v188, 0x206d0
	v_mov_b32_e32 v189, 0x206f0
	s_mov_b32 s26, 0xc2200000
	s_mov_b32 s27, 0xf149f2ca
	v_mov_b32_e32 v192, 0xba83126f
	s_mov_b32 s4, 0
	s_mov_b32 s28, 0
	v_mov_b64_e32 v[60:61], v[44:45]
	v_mov_b64_e32 v[58:59], v[42:43]
	v_mov_b64_e32 v[56:57], v[40:41]
	v_mov_b64_e32 v[54:55], v[38:39]
	v_mov_b64_e32 v[52:53], v[36:37]
	v_mov_b64_e32 v[50:51], v[34:35]
	v_mov_b64_e32 v[48:49], v[32:33]
	v_mov_b64_e32 v[2:3], v[34:35]
	v_mov_b64_e32 v[4:5], v[36:37]
	v_mov_b64_e32 v[6:7], v[38:39]
	v_mov_b64_e32 v[8:9], v[40:41]
	v_mov_b64_e32 v[10:11], v[42:43]
	v_mov_b64_e32 v[12:13], v[44:45]
	v_mov_b64_e32 v[14:15], v[46:47]
	v_mov_b64_e32 v[18:19], v[34:35]
	v_mov_b64_e32 v[20:21], v[36:37]
	v_mov_b64_e32 v[22:23], v[38:39]
	v_mov_b64_e32 v[24:25], v[40:41]
	v_mov_b64_e32 v[26:27], v[42:43]
	v_mov_b64_e32 v[28:29], v[44:45]
	v_mov_b64_e32 v[30:31], v[46:47]
.LBB2_9:
	s_cmp_lg_u32 s23, 0
	s_cselect_b64 s[14:15], -1, 0
	s_and_b64 vcc, exec, s[14:15]
	s_mov_b64 s[16:17], -1
	s_cbranch_vccz .LBB2_11
	s_cmp_eq_u32 s23, 1
	s_cbranch_scc1 .Lattn_wb8
	s_waitcnt vmcnt(0) lgkmcnt(0)
	s_barrier
	s_branch .Lattn_wb_done
.Lattn_wb8:
	s_waitcnt vmcnt(8) lgkmcnt(0)
	s_barrier
.Lattn_wb_done:
	s_mov_b64 s[16:17], 0

.LBB2_19:
	s_andn2_b64 vcc, exec, s[14:15]
	s_cbranch_vccnz .LBB2_22
	s_mov_b32 s5, 11
	s_branch .LBB2_22

.LBB2_38:
	s_cmp_lg_u32 s23, 0
	s_cbranch_scc1 .Lattn_diag_skip
	s_waitcnt vmcnt(8)
	s_sub_i32 s46, s20, s42
	s_abs_i32 s46, s46
	s_sub_i32 s47, s20, s43
	s_abs_i32 s47, s47
	s_lshl_b32 s46, s46, 6
	s_lshl_b32 s47, s47, 6
	s_add_i32 s46, s46, 0x20000
	s_add_i32 s47, s47, 0x20000
	v_mov_b32_e32 v64, s46
	v_mov_b32_e32 v65, s47
	ds_read_b64 v[66:67], v64
	ds_read_b64 v[68:69], v65
	s_lshl_b32 s46, s42, 4
	s_lshl_b32 s47, s43, 4
	s_add_i32 s46, s46, 0x20600
	s_add_i32 s47, s47, 0x20600
	v_mov_b32_e32 v64, s46
	v_mov_b32_e32 v65, s47
	ds_read_b128 v[70:73], v64
	ds_read_b128 v[74:77], v65
	v_fma_mix_f32 v78, v96, v210, 0 op_sel_hi:[1,1,0]
	v_fma_mix_f32 v79, v96, v226, 0 op_sel_hi:[1,1,0]
	v_fma_mix_f32 v78, v96, v210, v78 op_sel:[1,1,0] op_sel_hi:[1,1,0]
	v_fma_mix_f32 v79, v96, v226, v79 op_sel:[1,1,0] op_sel_hi:[1,1,0]
	v_fma_mix_f32 v78, v97, v211, v78 op_sel_hi:[1,1,0]
	v_fma_mix_f32 v79, v97, v227, v79 op_sel_hi:[1,1,0]
	v_fma_mix_f32 v78, v97, v211, v78 op_sel:[1,1,0] op_sel_hi:[1,1,0]
	v_fma_mix_f32 v79, v97, v227, v79 op_sel:[1,1,0] op_sel_hi:[1,1,0]
	v_fma_mix_f32 v78, v98, v212, v78 op_sel_hi:[1,1,0]
	v_fma_mix_f32 v79, v98, v228, v79 op_sel_hi:[1,1,0]
	v_fma_mix_f32 v78, v98, v212, v78 op_sel:[1,1,0] op_sel_hi:[1,1,0]
	v_fma_mix_f32 v79, v98, v228, v79 op_sel:[1,1,0] op_sel_hi:[1,1,0]
	v_fma_mix_f32 v78, v99, v213, v78 op_sel_hi:[1,1,0]
	v_fma_mix_f32 v79, v99, v229, v79 op_sel_hi:[1,1,0]
	v_fma_mix_f32 v78, v99, v213, v78 op_sel:[1,1,0] op_sel_hi:[1,1,0]
	v_fma_mix_f32 v79, v99, v229, v79 op_sel:[1,1,0] op_sel_hi:[1,1,0]
	v_fma_mix_f32 v78, v100, v214, v78 op_sel_hi:[1,1,0]
	v_fma_mix_f32 v79, v100, v230, v79 op_sel_hi:[1,1,0]
	v_fma_mix_f32 v78, v100, v214, v78 op_sel:[1,1,0] op_sel_hi:[1,1,0]
	v_fma_mix_f32 v79, v100, v230, v79 op_sel:[1,1,0] op_sel_hi:[1,1,0]
	v_fma_mix_f32 v78, v101, v215, v78 op_sel_hi:[1,1,0]
	v_fma_mix_f32 v79, v101, v231, v79 op_sel_hi:[1,1,0]
	v_fma_mix_f32 v78, v101, v215, v78 op_sel:[1,1,0] op_sel_hi:[1,1,0]
	v_fma_mix_f32 v79, v101, v231, v79 op_sel:[1,1,0] op_sel_hi:[1,1,0]
	v_fma_mix_f32 v78, v102, v216, v78 op_sel_hi:[1,1,0]
	v_fma_mix_f32 v79, v102, v232, v79 op_sel_hi:[1,1,0]
	v_fma_mix_f32 v78, v102, v216, v78 op_sel:[1,1,0] op_sel_hi:[1,1,0]
	v_fma_mix_f32 v79, v102, v232, v79 op_sel:[1,1,0] op_sel_hi:[1,1,0]
	v_fma_mix_f32 v78, v103, v217, v78 op_sel_hi:[1,1,0]
	v_fma_mix_f32 v79, v103, v233, v79 op_sel_hi:[1,1,0]
	v_fma_mix_f32 v78, v103, v217, v78 op_sel:[1,1,0] op_sel_hi:[1,1,0]
	v_fma_mix_f32 v79, v103, v233, v79 op_sel:[1,1,0] op_sel_hi:[1,1,0]
	v_fma_mix_f32 v78, v104, v218, v78 op_sel_hi:[1,1,0]
	v_fma_mix_f32 v79, v104, v234, v79 op_sel_hi:[1,1,0]
	v_fma_mix_f32 v78, v104, v218, v78 op_sel:[1,1,0] op_sel_hi:[1,1,0]
	v_fma_mix_f32 v79, v104, v234, v79 op_sel:[1,1,0] op_sel_hi:[1,1,0]
	v_fma_mix_f32 v78, v105, v219, v78 op_sel_hi:[1,1,0]
	v_fma_mix_f32 v79, v105, v235, v79 op_sel_hi:[1,1,0]
	v_fma_mix_f32 v78, v105, v219, v78 op_sel:[1,1,0] op_sel_hi:[1,1,0]
	v_fma_mix_f32 v79, v105, v235, v79 op_sel:[1,1,0] op_sel_hi:[1,1,0]
	v_fma_mix_f32 v78, v106, v220, v78 op_sel_hi:[1,1,0]
	v_fma_mix_f32 v79, v106, v236, v79 op_sel_hi:[1,1,0]
	v_fma_mix_f32 v78, v106, v220, v78 op_sel:[1,1,0] op_sel_hi:[1,1,0]
	v_fma_mix_f32 v79, v106, v236, v79 op_sel:[1,1,0] op_sel_hi:[1,1,0]
	v_fma_mix_f32 v78, v107, v221, v78 op_sel_hi:[1,1,0]
	v_fma_mix_f32 v79, v107, v237, v79 op_sel_hi:[1,1,0]
	v_fma_mix_f32 v78, v107, v221, v78 op_sel:[1,1,0] op_sel_hi:[1,1,0]
	v_fma_mix_f32 v79, v107, v237, v79 op_sel:[1,1,0] op_sel_hi:[1,1,0]
	v_fma_mix_f32 v78, v108, v222, v78 op_sel_hi:[1,1,0]
	v_fma_mix_f32 v79, v108, v238, v79 op_sel_hi:[1,1,0]
	v_fma_mix_f32 v78, v108, v222, v78 op_sel:[1,1,0] op_sel_hi:[1,1,0]
	v_fma_mix_f32 v79, v108, v238, v79 op_sel:[1,1,0] op_sel_hi:[1,1,0]
	v_fma_mix_f32 v78, v109, v223, v78 op_sel_hi:[1,1,0]
	v_fma_mix_f32 v79, v109, v239, v79 op_sel_hi:[1,1,0]
	v_fma_mix_f32 v78, v109, v223, v78 op_sel:[1,1,0] op_sel_hi:[1,1,0]
	v_fma_mix_f32 v79, v109, v239, v79 op_sel:[1,1,0] op_sel_hi:[1,1,0]
	v_fma_mix_f32 v78, v110, v224, v78 op_sel_hi:[1,1,0]
	v_fma_mix_f32 v79, v110, v240, v79 op_sel_hi:[1,1,0]
	v_fma_mix_f32 v78, v110, v224, v78 op_sel:[1,1,0] op_sel_hi:[1,1,0]
	v_fma_mix_f32 v79, v110, v240, v79 op_sel:[1,1,0] op_sel_hi:[1,1,0]
	v_fma_mix_f32 v78, v111, v225, v78 op_sel_hi:[1,1,0]
	v_fma_mix_f32 v79, v111, v241, v79 op_sel_hi:[1,1,0]
	v_fma_mix_f32 v78, v111, v225, v78 op_sel:[1,1,0] op_sel_hi:[1,1,0]
	v_fma_mix_f32 v79, v111, v241, v79 op_sel:[1,1,0] op_sel_hi:[1,1,0]
	v_mov_b32_e32 v64, v78
	v_mov_b32_e32 v65, v79
	s_nop 1
	v_permlane32_swap_b32_e32 v78, v64
	v_permlane32_swap_b32_e32 v79, v65
	v_add_f32_e32 v78, v78, v64
	v_add_f32_e32 v79, v79, v65
	s_waitcnt lgkmcnt(0)
	v_add_f32_e32 v78, v78, v48
	v_add_f32_e32 v79, v79, v48
	v_add_f32_e32 v78, v78, v66
	v_add_f32_e32 v79, v79, v68
	s_mov_b32 s48, 0xc2200a3d
	v_cmp_ngt_f32_e32 vcc, s48, v78
	s_cmp_lg_u64 vcc, 0
	s_cselect_b32 s50, 4, 0
	v_cmp_ngt_f32_e32 vcc, s48, v79
	s_cmp_lg_u64 vcc, 0
	s_cselect_b32 s51, 0x400, 0
	s_or_b32 s50, s50, s51
	v_max3_f32 v64, v70, v71, v72
	v_max_f32_e32 v64, v64, v73
	v_fma_f32 v64, v169, v64, v67
	v_sub_f32_e32 v64, v64, v193
	v_cmp_ngt_f32_e32 vcc, s48, v64
	s_cmp_lg_u64 vcc, 0
	s_cselect_b32 s51, 4, 0
	s_or_b32 s50, s50, s51
	v_max3_f32 v65, v74, v75, v76
	v_max_f32_e32 v65, v65, v77
	v_fma_f32 v65, v169, v65, v69
	v_sub_f32_e32 v65, v65, v193
	v_cmp_ngt_f32_e32 vcc, s48, v65
	s_cmp_lg_u64 vcc, 0
	s_cselect_b32 s51, 0x400, 0
	s_or_b32 s50, s50, s51
	v_mov_b32_e32 v64, s25
	v_mov_b32_e32 v65, s50
	ds_write_b32 v64, v65 offset:32
.Lattn_diag_skip:
	s_cmp_lg_u32 s5, 11
	s_cbranch_scc1 .Lattn_pre_skip
	s_not_b32 s46, s23
	s_lshl_b32 s46, s46, 16
	s_and_b32 s46, s46, 0x10000
	v_or_b32_e32 v33, s46, v175
	s_waitcnt vmcnt(7)
	ds_write_b128 v33, v[112:115]
	s_waitcnt vmcnt(6)
	ds_write_b128 v33, v[116:119] offset:8192
	s_waitcnt vmcnt(5)
	ds_write_b128 v33, v[120:123] offset:16384
	s_waitcnt vmcnt(4)
	ds_write_b128 v33, v[124:127] offset:24576
	s_waitcnt vmcnt(3)
	ds_write_b128 v33, v[128:131] offset:32768
	s_waitcnt vmcnt(2)
	ds_write_b128 v33, v[132:135] offset:40960
	s_waitcnt vmcnt(1)
	ds_write_b128 v33, v[136:139] offset:49152
	s_waitcnt vmcnt(0)
	ds_write_b128 v33, v[140:143] offset:57344
